# v52 + NSA block-compression K loop software-pipelined (8 operand pairs in flight instead of one round trip per MFMA), w2 GEMM loads issued up front
# baseline (speedup 1.0000x reference)
.LBB0_3774:
	s_andn2_b64 vcc, exec, s[6:7]
	s_cbranch_vccnz .LBB0_3601
	s_bfe_u32 s2, s69, 0x40002
	s_bfe_u32 s0, s33, 0x20006
	s_ashr_i32 s8, s33, 8
	s_cmp_lt_u32 s69, 64
	s_cselect_b64 s[4:5], -1, 0
	s_and_b64 s[6:7], s[4:5], exec
	s_mov_b32 s3, 0x25e00000
	s_cselect_b32 s9, s3, 0x26700000
	s_lshl_b32 s3, s69, 1
	s_and_b32 s3, s3, 0xffffff80
	s_lshl_b32 s6, s8, 11
	s_add_i32 s10, s3, s63
	s_lshl_b32 s3, s0, 5
	v_and_b32_e32 v24, 31, v154
	s_ashr_i32 s7, s6, 31
	s_or_b32 s10, s3, s10
	s_lshl_b32 s12, s2, 19
	v_or_b32_e32 v18, s10, v24
	s_lshl_b64 s[6:7], s[6:7], 1
	v_readlane_b32 s10, v255, 32
	v_ashrrev_i32_e32 v19, 31, v18
	v_lshrrev_b32_e32 v0, 1, v154
	s_add_u32 s10, s10, s6
	v_readlane_b32 s11, v255, 33
	v_lshlrev_b64 v[2:3], 13, v[18:19]
	v_and_b32_e32 v0, 16, v0
	s_addc_u32 s11, s11, s7
	v_or_b32_e32 v2, v2, v0
	s_add_u32 s9, s9, s12
	v_lshl_add_u64 v[20:21], s[10:11], 0, v[2:3]
	s_addc_u32 s10, 0, 0
	s_add_u32 s6, s6, s9
	s_addc_u32 s7, s7, s10
	v_or_b32_e32 v2, s6, v0
	s_and_b32 s6, s69, 3
	v_lshlrev_b32_e32 v0, 12, v24
	v_mov_b32_e32 v3, s7
	v_lshl_or_b32 v0, s6, 17, v0
	v_lshl_add_u64 v[2:3], v[2:3], 0, v[0:1]
	v_lshl_add_u64 v[22:23], s[84:85], 0, v[2:3]
	v_mov_b32_e32 v2, 0
	s_mov_b64 s[6:7], 0
	v_mov_b32_e32 v3, v2
	v_mov_b32_e32 v4, v2
	v_mov_b32_e32 v5, v2
	v_mov_b32_e32 v6, v2
	v_mov_b32_e32 v7, v2
	v_mov_b32_e32 v8, v2
	v_mov_b32_e32 v9, v2
	v_mov_b32_e32 v10, v2
	v_mov_b32_e32 v11, v2
	v_mov_b32_e32 v12, v2
	v_mov_b32_e32 v13, v2
	v_mov_b32_e32 v14, v2
	v_mov_b32_e32 v15, v2
	v_mov_b32_e32 v16, v2
	v_mov_b32_e32 v17, v2
	global_load_dwordx4 v[28:31], v[22:23], off
	global_load_dwordx4 v[32:35], v[20:21], off offset:-256
	global_load_dwordx4 v[36:39], v[22:23], off offset:32
	global_load_dwordx4 v[40:43], v[20:21], off offset:-224
	global_load_dwordx4 v[44:47], v[22:23], off offset:64
	global_load_dwordx4 v[48:51], v[20:21], off offset:-192
	global_load_dwordx4 v[52:55], v[22:23], off offset:96
	global_load_dwordx4 v[56:59], v[20:21], off offset:-160
	global_load_dwordx4 v[156:159], v[22:23], off offset:128
	global_load_dwordx4 v[160:163], v[20:21], off offset:-128
	global_load_dwordx4 v[164:167], v[22:23], off offset:160
	global_load_dwordx4 v[168:171], v[20:21], off offset:-96
	global_load_dwordx4 v[172:175], v[22:23], off offset:192
	global_load_dwordx4 v[176:179], v[20:21], off offset:-64
	global_load_dwordx4 v[180:183], v[22:23], off offset:224
	global_load_dwordx4 v[184:187], v[20:21], off offset:-32
.LBB0_3776:
	v_lshl_add_u64 v[26:27], v[22:23], 0, s[6:7]
	v_lshl_add_u64 v[60:61], v[20:21], 0, s[6:7]
	s_add_u32 s6, s6, 0x100
	s_addc_u32 s7, s7, 0
	s_cmpk_eq_i32 s6, 0xf00
	s_waitcnt vmcnt(14)
	v_mfma_f32_32x32x16_bf16 v[2:17], v[28:31], v[32:35], v[2:17]
	global_load_dwordx4 v[28:31], v[26:27], off offset:256
	global_load_dwordx4 v[32:35], v[60:61], off
	s_waitcnt vmcnt(14)
	v_mfma_f32_32x32x16_bf16 v[2:17], v[36:39], v[40:43], v[2:17]
	global_load_dwordx4 v[36:39], v[26:27], off offset:288
	global_load_dwordx4 v[40:43], v[60:61], off offset:32
	s_waitcnt vmcnt(14)
	v_mfma_f32_32x32x16_bf16 v[2:17], v[44:47], v[48:51], v[2:17]
	global_load_dwordx4 v[44:47], v[26:27], off offset:320
	global_load_dwordx4 v[48:51], v[60:61], off offset:64
	s_waitcnt vmcnt(14)
	v_mfma_f32_32x32x16_bf16 v[2:17], v[52:55], v[56:59], v[2:17]
	global_load_dwordx4 v[52:55], v[26:27], off offset:352
	global_load_dwordx4 v[56:59], v[60:61], off offset:96
	s_waitcnt vmcnt(14)
	v_mfma_f32_32x32x16_bf16 v[2:17], v[156:159], v[160:163], v[2:17]
	global_load_dwordx4 v[156:159], v[26:27], off offset:384
	global_load_dwordx4 v[160:163], v[60:61], off offset:128
	s_waitcnt vmcnt(14)
	v_mfma_f32_32x32x16_bf16 v[2:17], v[164:167], v[168:171], v[2:17]
	global_load_dwordx4 v[164:167], v[26:27], off offset:416
	global_load_dwordx4 v[168:171], v[60:61], off offset:160
	s_waitcnt vmcnt(14)
	v_mfma_f32_32x32x16_bf16 v[2:17], v[172:175], v[176:179], v[2:17]
	global_load_dwordx4 v[172:175], v[26:27], off offset:448
	global_load_dwordx4 v[176:179], v[60:61], off offset:192
	s_waitcnt vmcnt(14)
	v_mfma_f32_32x32x16_bf16 v[2:17], v[180:183], v[184:187], v[2:17]
	global_load_dwordx4 v[180:183], v[26:27], off offset:480
	global_load_dwordx4 v[184:187], v[60:61], off offset:224
	s_cbranch_scc0 .LBB0_3776
	s_waitcnt vmcnt(14)
	v_mfma_f32_32x32x16_bf16 v[2:17], v[28:31], v[32:35], v[2:17]
	s_waitcnt vmcnt(12)
	v_mfma_f32_32x32x16_bf16 v[2:17], v[36:39], v[40:43], v[2:17]
	s_waitcnt vmcnt(10)
	v_mfma_f32_32x32x16_bf16 v[2:17], v[44:47], v[48:51], v[2:17]
	s_waitcnt vmcnt(8)
	v_mfma_f32_32x32x16_bf16 v[2:17], v[52:55], v[56:59], v[2:17]
	s_waitcnt vmcnt(6)
	v_mfma_f32_32x32x16_bf16 v[2:17], v[156:159], v[160:163], v[2:17]
	s_waitcnt vmcnt(4)
	v_mfma_f32_32x32x16_bf16 v[2:17], v[164:167], v[168:171], v[2:17]
	s_waitcnt vmcnt(2)
	v_mfma_f32_32x32x16_bf16 v[2:17], v[172:175], v[176:179], v[2:17]
	s_waitcnt vmcnt(0)
	v_mfma_f32_32x32x16_bf16 v[2:17], v[180:183], v[184:187], v[2:17]
	s_cmp_lg_u32 s8, 1
	s_cbranch_scc1 .LBB0_3779
	s_lshl_b32 s0, s0, 12
	s_add_i32 s0, s0, 0
	v_lshl_add_u32 v0, v153, 2, s0
	s_nop 5
	ds_write2st64_b32 v0, v2, v3 offset1:1
	ds_write2st64_b32 v0, v4, v5 offset0:2 offset1:3
	ds_write2st64_b32 v0, v6, v7 offset0:4 offset1:5
	ds_write2st64_b32 v0, v8, v9 offset0:6 offset1:7
	ds_write2st64_b32 v0, v10, v11 offset0:8 offset1:9
	ds_write2st64_b32 v0, v12, v13 offset0:10 offset1:11
	ds_write2st64_b32 v0, v14, v15 offset0:12 offset1:13
	ds_write2st64_b32 v0, v16, v17 offset0:14 offset1:15

.LBB0_3781:
	s_andn2_b64 vcc, exec, s[6:7]
	s_waitcnt lgkmcnt(0)
	s_barrier
	s_cbranch_vccnz .LBB0_3783
	v_readlane_b32 s6, v255, 30
	v_lshlrev_b64 v[2:3], 8, v[18:19]
	v_readlane_b32 s7, v255, 31
	v_lshlrev_b32_e32 v0, 4, v21
	s_lshl_b32 s0, s69, 5
	v_lshl_add_u64 v[2:3], s[6:7], 0, v[2:3]
	v_lshl_add_u64 v[18:19], v[2:3], 0, v[0:1]
	v_mul_u32_u24_e32 v2, 0x110, v24
	v_add3_u32 v0, 0, v2, v0
	global_load_dwordx4 v[28:31], v[18:19], off
	global_load_dwordx4 v[32:35], v[18:19], off offset:32
	global_load_dwordx4 v[36:39], v[18:19], off offset:64
	global_load_dwordx4 v[40:43], v[18:19], off offset:96
	global_load_dwordx4 v[44:47], v[18:19], off offset:128
	global_load_dwordx4 v[48:51], v[18:19], off offset:160
	global_load_dwordx4 v[52:55], v[18:19], off offset:192
	global_load_dwordx4 v[56:59], v[18:19], off offset:224
	ds_read_b128 v[156:159], v0 offset:16384
	ds_read_b128 v[160:163], v0 offset:16416
	ds_read_b128 v[164:167], v0 offset:16448
	ds_read_b128 v[168:171], v0 offset:16480
	ds_read_b128 v[172:175], v0 offset:16512
	ds_read_b128 v[176:179], v0 offset:16544
	ds_read_b128 v[180:183], v0 offset:16576
	ds_read_b128 v[184:187], v0 offset:16608
	s_and_b32 s0, s0, 0x60
	s_and_b64 s[4:5], s[4:5], exec
	s_mov_b32 s4, 0x2c200000
	s_cselect_b32 s4, s4, 0x2c300000
	v_readlane_b32 s5, v255, 16
	s_add_u32 s4, s5, s4
	v_readlane_b32 s5, v255, 18
	s_addc_u32 s5, s5, 0
	s_lshl_b32 s2, s2, 15
	s_add_u32 s2, s4, s2
	s_addc_u32 s4, s5, 0
	s_waitcnt vmcnt(7) lgkmcnt(7)
	v_mfma_f32_32x32x16_bf16 v[2:17], v[156:159], v[28:31], 0
	s_waitcnt vmcnt(6) lgkmcnt(6)
	v_mfma_f32_32x32x16_bf16 v[2:17], v[160:163], v[32:35], v[2:17]
	s_waitcnt vmcnt(5) lgkmcnt(5)
	v_mfma_f32_32x32x16_bf16 v[2:17], v[164:167], v[36:39], v[2:17]
	s_waitcnt vmcnt(4) lgkmcnt(4)
	v_mfma_f32_32x32x16_bf16 v[2:17], v[168:171], v[40:43], v[2:17]
	s_waitcnt vmcnt(3) lgkmcnt(3)
	v_mfma_f32_32x32x16_bf16 v[2:17], v[172:175], v[44:47], v[2:17]
	s_waitcnt vmcnt(2) lgkmcnt(2)
	v_mfma_f32_32x32x16_bf16 v[2:17], v[176:179], v[48:51], v[2:17]
	s_waitcnt vmcnt(1) lgkmcnt(1)
	v_mfma_f32_32x32x16_bf16 v[2:17], v[180:183], v[52:55], v[2:17]
	s_waitcnt vmcnt(0) lgkmcnt(0)
	v_mfma_f32_32x32x16_bf16 v[2:17], v[184:187], v[56:59], v[2:17]
	v_lshl_or_b32 v22, v21, 2, s0
	s_lshl_b32 s0, s3, 1
	s_add_u32 s2, s2, s0
	s_addc_u32 s3, s4, 0
	v_mov_b32_e32 v21, v1
	v_lshl_add_u64 v[18:19], s[2:3], 0, v[20:21]
	v_lshlrev_b32_e32 v0, 8, v22
	v_lshl_add_u64 v[18:19], v[18:19], 0, v[0:1]
	s_nop 3
	v_bfe_u32 v0, v2, 16, 1
	s_movk_i32 s2, 0x7fff
	v_add3_u32 v0, v2, v0, s2
	v_lshrrev_b32_e32 v0, 16, v0
	global_store_short v[18:19], v0, off sc1
	v_bfe_u32 v0, v3, 16, 1
	v_add3_u32 v0, v3, v0, s2
	v_lshrrev_b32_e32 v0, 16, v0
	global_store_short v[18:19], v0, off offset:256 sc1
	v_bfe_u32 v0, v4, 16, 1
	v_add3_u32 v0, v4, v0, s2
	v_lshrrev_b32_e32 v0, 16, v0
	global_store_short v[18:19], v0, off offset:512 sc1
	v_bfe_u32 v0, v5, 16, 1
	v_add3_u32 v0, v5, v0, s2
	v_lshrrev_b32_e32 v0, 16, v0
	global_store_short v[18:19], v0, off offset:768 sc1
	v_bfe_u32 v0, v6, 16, 1
	v_add3_u32 v0, v6, v0, s2
	v_lshrrev_b32_e32 v0, 16, v0
	global_store_short v[18:19], v0, off offset:2048 sc1
	v_bfe_u32 v0, v7, 16, 1
	v_add3_u32 v0, v7, v0, s2
	v_lshrrev_b32_e32 v0, 16, v0
	global_store_short v[18:19], v0, off offset:2304 sc1
	v_bfe_u32 v0, v8, 16, 1
	v_add3_u32 v0, v8, v0, s2
	v_lshrrev_b32_e32 v0, 16, v0
	global_store_short v[18:19], v0, off offset:2560 sc1
	v_bfe_u32 v0, v9, 16, 1
	v_add3_u32 v0, v9, v0, s2
	v_lshrrev_b32_e32 v0, 16, v0
	global_store_short v[18:19], v0, off offset:2816 sc1
	v_bfe_u32 v0, v10, 16, 1
	s_movk_i32 s0, 0x1000
	v_add3_u32 v0, v10, v0, s2
	v_add_co_u32_e32 v2, vcc, s0, v18
	v_lshrrev_b32_e32 v0, 16, v0
	s_nop 0
	v_addc_co_u32_e32 v3, vcc, 0, v19, vcc
	global_store_short v[2:3], v0, off sc1
	v_bfe_u32 v0, v11, 16, 1
	v_add3_u32 v0, v11, v0, s2
	v_lshrrev_b32_e32 v0, 16, v0
	global_store_short v[2:3], v0, off offset:256 sc1
	v_bfe_u32 v0, v12, 16, 1
	v_add3_u32 v0, v12, v0, s2
	v_lshrrev_b32_e32 v0, 16, v0
	global_store_short v[2:3], v0, off offset:512 sc1
	v_bfe_u32 v0, v13, 16, 1
	v_add3_u32 v0, v13, v0, s2
	v_lshrrev_b32_e32 v0, 16, v0
	global_store_short v[2:3], v0, off offset:768 sc1
	v_bfe_u32 v0, v14, 16, 1
	v_add3_u32 v0, v14, v0, s2
	v_lshrrev_b32_e32 v0, 16, v0
	global_store_short v[2:3], v0, off offset:2048 sc1
	v_bfe_u32 v0, v15, 16, 1
	v_add3_u32 v0, v15, v0, s2
	v_lshrrev_b32_e32 v0, 16, v0
	global_store_short v[2:3], v0, off offset:2304 sc1
	v_bfe_u32 v0, v16, 16, 1
	v_add3_u32 v0, v16, v0, s2
	v_lshrrev_b32_e32 v0, 16, v0
	global_store_short v[2:3], v0, off offset:2560 sc1
	v_bfe_u32 v0, v17, 16, 1
	s_movk_i32 s0, 0x64
	v_add3_u32 v0, v17, v0, s2
	v_cmp_ne_u32_e32 vcc, s0, v22
	s_nop 1
	v_cndmask_b32_sdwa v0, v1, v0, vcc dst_sel:DWORD dst_unused:UNUSED_PAD src0_sel:DWORD src1_sel:WORD_1
	global_store_short v[2:3], v0, off offset:2816 sc1
